# speedup vs baseline: 1.0308x; 1.0045x over previous
.Lh_no_out:
	s_cmp_eq_u32 s17, 0
	s_cselect_b32 s4, s4, s6
	s_cselect_b32 s5, s5, s7
	s_add_u32 s24, s8, s22
	s_addc_u32 s25, s9, 0
	s_add_u32 s4, s4, s21
	s_addc_u32 s5, s5, 0
	global_load_dwordx4 v[14:17], v18, s[24:25] nt
	global_load_dwordx4 v[2:5], v18, s[4:5] nt
	s_add_u32 s6, s4, 0x40000
	s_addc_u32 s7, s5, 0
	s_add_u32 s8, s4, 0x80000
	s_addc_u32 s9, s5, 0
	s_barrier
	global_load_dwordx4 v[6:9], v18, s[6:7] nt
	s_barrier
	global_load_dwordx4 v[10:13], v18, s[8:9] nt
	s_mul_i32 s46, s3, 0xc00
	s_add_u32 s46, s46, 0x8420
	v_lshl_add_u32 v26, v1, 2, s46
	v_and_b32_e32 v38, 15, v0
	s_mul_i32 s58, s17, 0x4200
	s_add_u32 s58, s58, 0x1e0
	v_lshl_add_u32 v38, v38, 2, s58
	v_add_u32_e32 v39, 0x1600, v38
	v_add_u32_e32 v40, 0x2c00, v38
	v_mov_b32_e32 v41, 0x41fc0000
	v_mov_b32_e32 v42, 0xbf38aa3b
	s_mov_b32 s48, 0x3f940000
	s_mov_b32 s51, 0x3fb8aa3b
	s_mov_b32 s42, 0
	s_mov_b32 s43, 0
	s_mov_b32 s44, 0x7fffffff
	s_mov_b32 s45, 0x7fffffff
	s_mov_b32 s47, 0
	s_mul_i32 s58, s3, 0x1600
	s_add_u32 s58, s58, 0x320
	v_lshl_add_u32 v44, v1, 6, s58
	v_bfe_u32 v45, v1, 2, 2
	v_lshlrev_b32_e32 v45, 4, v45
	v_xor_b32_e32 v46, 16, v45
	v_xor_b32_e32 v47, 32, v45
	v_xor_b32_e32 v48, 48, v45
	v_add_u32_e32 v45, v44, v45
	v_add_u32_e32 v46, v44, v46
	v_add_u32_e32 v47, v44, v47
	v_add_u32_e32 v48, v44, v48
	s_mul_i32 s58, s2, 0x600
	s_lshl_b32 s59, s3, 8
	s_add_u32 s58, s58, s59
	s_add_u32 s10, s10, s58
	s_addc_u32 s11, s11, 0
	v_lshlrev_b32_e32 v49, 2, v1
	s_lshl_b32 s58, s2, 2
	s_add_u32 s12, s12, s58
	s_addc_u32 s13, s13, 0
	s_setprio 3
	s_cmp_lt_u32 s3, 8
	s_cbranch_scc1 .Lh_nostagger
	s_sleep 3
.Lh_nostagger:
	s_waitcnt vmcnt(3)
	v_cmp_lt_f32_e64 s[26:27], 0.5, v14
	v_cmp_lt_f32_e64 s[28:29], 0.5, v15
	v_cmp_lt_f32_e64 s[30:31], 0.5, v16
	v_cmp_lt_f32_e64 s[32:33], 0.5, v17
	s_cmp_lg_u32 s17, 0
	s_cbranch_scc1 .Lh_no_cnt
	s_bcnt1_i32_b64 s54, s[26:27]
	s_bcnt1_i32_b64 s55, s[28:29]
	s_bcnt1_i32_b64 s56, s[30:31]
	s_bcnt1_i32_b64 s57, s[32:33]
	s_add_i32 s54, s54, s55
	s_add_i32 s56, s56, s57
	s_add_i32 s54, s54, s56
	s_lshl_b32 s55, s16, 2
	v_mov_b32_e32 v36, s55
	v_mov_b32_e32 v37, s54
	s_mov_b64 exec, 1
	ds_write_b32 v36, v37
	s_mov_b64 exec, -1
